# combined: hot-path rescale flag clear plus reordered row-max reduction on the slim-DMA aligned base
# baseline (speedup 1.0000x reference)
.LBB0_726:
	v_add_u32_e64 v164, s18, v239
	s_add_i32 m0, s38, s30
	s_nop 0
	global_load_lds_dwordx4 v244, s[98:99]
	s_add_i32 m0, s22, s31
	s_nop 0
	global_load_lds_dwordx4 v245, s[98:99]
	s_add_u32 s98, s98, 0x20000
	s_addc_u32 s99, s99, 0
	s_nop 0
	ds_read_b64_tr_b16 v[190:191], v164 offset:24576
	ds_read_b64_tr_b16 v[192:193], v164 offset:25088
	s_waitcnt lgkmcnt(2)
	s_nop 0
	v_mfma_f32_32x32x16_bf16 v[48:63], v[158:161], v[110:113], v[48:63]
	v_add_f32_e32 v114, v80, v81
	v_add_f32_e32 v114, v82, v114
	v_add_f32_e32 v114, v83, v114
	v_add_f32_e32 v114, v84, v114
	v_add_f32_e64 v114, v85, v114
	v_cvt_pk_bf16_f32 v126, v80, v81
	v_cvt_pk_bf16_f32 v127, v82, v83
	ds_read_b64_tr_b16 v[186:187], v164 offset:28672
	ds_read_b64_tr_b16 v[188:189], v164 offset:29184
	v_mfma_f32_32x32x16_bf16 v[32:47], v[146:149], v[110:113], v[32:47]
	v_add_f32_e32 v80, v86, v114
	v_add_f32_e32 v80, v87, v80
	v_add_f32_e32 v80, v88, v80
	v_add_f32_e32 v80, v89, v80
	v_cvt_pk_bf16_f32 v128, v84, v85
	v_cvt_pk_bf16_f32 v129, v86, v87
	ds_read_b64_tr_b16 v[182:183], v164 offset:25600
	ds_read_b64_tr_b16 v[184:185], v164 offset:26112
	v_mfma_f32_32x32x16_bf16 v[48:63], v[154:157], v[106:109], v[48:63]
	v_add_f32_e32 v80, v90, v80
	v_add_f32_e32 v80, v91, v80
	v_add_f32_e32 v80, v92, v80
	v_add_f32_e32 v80, v93, v80
	v_cvt_pk_bf16_f32 v122, v88, v89
	v_cvt_pk_bf16_f32 v123, v90, v91
	ds_read_b64_tr_b16 v[178:179], v164 offset:29696
	ds_read_b64_tr_b16 v[180:181], v164 offset:30208
	v_mfma_f32_32x32x16_bf16 v[32:47], v[142:145], v[106:109], v[32:47]
	v_add_f32_e32 v80, v94, v80
	v_add_f32_e32 v80, v95, v80
	v_add_f32_e32 v80, v64, v80
	v_add_f32_e32 v80, v65, v80
	v_cvt_pk_bf16_f32 v124, v92, v93
	v_cvt_pk_bf16_f32 v125, v94, v95
	ds_read_b64_tr_b16 v[166:167], v164 offset:26624
	ds_read_b64_tr_b16 v[168:169], v164 offset:27136
	v_mfma_f32_32x32x16_bf16 v[48:63], v[150:153], v[102:105], v[48:63]
	v_add_f32_e32 v80, v66, v80
	v_add_f32_e32 v80, v67, v80
	v_add_f32_e32 v80, v68, v80
	v_add_f32_e32 v80, v69, v80
	v_cvt_pk_bf16_f32 v118, v64, v65
	v_cvt_pk_bf16_f32 v119, v66, v67
	ds_read_b64_tr_b16 v[174:175], v164 offset:30720
	ds_read_b64_tr_b16 v[176:177], v164 offset:31232
	v_mfma_f32_32x32x16_bf16 v[32:47], v[138:141], v[102:105], v[32:47]
	v_add_f32_e32 v64, v70, v80
	v_add_f32_e32 v64, v71, v64
	v_add_f32_e32 v64, v72, v64
	v_add_f32_e32 v64, v73, v64
	v_cvt_pk_bf16_f32 v120, v68, v69
	v_cvt_pk_bf16_f32 v121, v70, v71
	ds_read_b64_tr_b16 v[170:171], v164 offset:27648
	ds_read_b64_tr_b16 v[172:173], v164 offset:28160
	v_mfma_f32_32x32x16_bf16 v[48:63], v[134:137], v[98:101], v[48:63]
	v_add_f32_e32 v64, v74, v64
	v_add_f32_e32 v64, v75, v64
	v_add_f32_e32 v64, v76, v64
	v_add_f32_e32 v64, v77, v64
	v_cvt_pk_bf16_f32 v114, v72, v73
	v_cvt_pk_bf16_f32 v115, v74, v75
	ds_read_b64_tr_b16 v[162:163], v164 offset:31744
	ds_read_b64_tr_b16 v[164:165], v164 offset:32256
	v_mfma_f32_32x32x16_bf16 v[32:47], v[130:133], v[98:101], v[32:47]
	v_add_f32_e32 v64, v78, v64
	v_add_f32_e32 v64, v79, v64
	v_add_f32_e64 v224, v240, v64
	v_cvt_pk_bf16_f32 v116, v76, v77
	v_cvt_pk_bf16_f32 v117, v78, v79
	s_waitcnt lgkmcnt(14)
	s_nop 0
	ds_read_b128 v[64:67], v205
	ds_read_b128 v[68:71], v205 offset:32
	ds_read_b128 v[82:85], v205 offset:128
	ds_read_b128 v[86:89], v205 offset:160
	ds_read_b128 v[72:75], v205 offset:64
	ds_read_b128 v[76:79], v205 offset:96
	ds_read_b128 v[90:93], v205 offset:192
	ds_read_b128 v[138:141], v205 offset:224
	v_max_f32_e64 v80, v48, v49
	v_max3_f32 v81, v50, v51, v52
	v_max3_f32 v80, v80, v53, v54
	v_max3_f32 v81, v81, v55, v56
	v_max3_f32 v80, v80, v57, v58
	v_max3_f32 v81, v81, v59, v60
	v_max3_f32 v80, v80, v61, v62
	v_max3_f32 v81, v81, v63, v32
	v_max3_f32 v80, v80, v33, v34
	v_max3_f32 v81, v81, v35, v36
	v_max3_f32 v80, v80, v37, v38
	v_max3_f32 v81, v81, v39, v40
	v_max3_f32 v80, v80, v41, v42
	v_max3_f32 v81, v81, v43, v44
	v_max3_f32 v80, v80, v45, v46
	v_max3_f32 v80, v80, v47, v81
	v_mov_b32_e64 v81, v80
	s_nop 1
	v_permlane32_swap_b32_e32 v80, v81
	v_max_f32_e32 v80, v80, v81
	v_cmp_lt_f32_e32 vcc, s51, v80
	s_mov_b64 s[18:19], 0
	s_cbranch_vccnz .LBB0_734

.LBB0_729:
	s_add_i32 s18, s22, 0x2000
	v_add_u32_e64 v162, s38, v239
	s_cmpk_lg_i32 s22, 0x4000
	s_cselect_b32 s38, s18, 0
	s_add_i32 m0, s22, s30
	s_nop 0
	global_load_lds_dwordx4 v244, s[98:99]
	s_add_i32 m0, s38, s31
	s_nop 0
	global_load_lds_dwordx4 v245, s[98:99]
	s_add_u32 s98, s98, 0x20000
	s_addc_u32 s99, s99, 0
	s_nop 0
	ds_read_b64_tr_b16 v[194:195], v162 offset:24576
	ds_read_b64_tr_b16 v[196:197], v162 offset:25088
	s_waitcnt lgkmcnt(2)
	s_nop 0
	v_mfma_f32_32x32x16_bf16 v[80:95], v[134:137], v[110:113], v[80:95]
	v_add_f32_e32 v114, v48, v49
	v_add_f32_e32 v114, v50, v114
	v_add_f32_e32 v114, v51, v114
	v_add_f32_e32 v114, v52, v114
	v_add_f32_e64 v114, v53, v114
	v_cvt_pk_bf16_f32 v126, v48, v49
	v_cvt_pk_bf16_f32 v127, v50, v51
	ds_read_b64_tr_b16 v[190:191], v162 offset:28672
	ds_read_b64_tr_b16 v[192:193], v162 offset:29184
	v_mfma_f32_32x32x16_bf16 v[64:79], v[130:133], v[110:113], v[64:79]
	v_add_f32_e32 v48, v54, v114
	v_add_f32_e32 v48, v55, v48
	v_add_f32_e32 v48, v56, v48
	v_add_f32_e32 v48, v57, v48
	v_cvt_pk_bf16_f32 v128, v52, v53
	v_cvt_pk_bf16_f32 v129, v54, v55
	ds_read_b64_tr_b16 v[186:187], v162 offset:25600
	ds_read_b64_tr_b16 v[188:189], v162 offset:26112
	v_mfma_f32_32x32x16_bf16 v[80:95], v[146:149], v[106:109], v[80:95]
	v_add_f32_e32 v48, v58, v48
	v_add_f32_e32 v48, v59, v48
	v_add_f32_e32 v48, v60, v48
	v_add_f32_e32 v48, v61, v48
	v_cvt_pk_bf16_f32 v122, v56, v57
	v_cvt_pk_bf16_f32 v123, v58, v59
	ds_read_b64_tr_b16 v[138:139], v162 offset:29696
	ds_read_b64_tr_b16 v[140:141], v162 offset:30208
	v_mfma_f32_32x32x16_bf16 v[64:79], v[142:145], v[106:109], v[64:79]
	v_add_f32_e32 v48, v62, v48
	v_add_f32_e32 v48, v63, v48
	v_add_f32_e32 v48, v32, v48
	v_add_f32_e32 v48, v33, v48
	v_cvt_pk_bf16_f32 v124, v60, v61
	v_cvt_pk_bf16_f32 v125, v62, v63
	ds_read_b64_tr_b16 v[182:183], v162 offset:26624
	ds_read_b64_tr_b16 v[184:185], v162 offset:27136
	v_mfma_f32_32x32x16_bf16 v[80:95], v[158:161], v[102:105], v[80:95]
	v_add_f32_e32 v48, v34, v48
	v_add_f32_e32 v48, v35, v48
	v_add_f32_e32 v48, v36, v48
	v_add_f32_e32 v48, v37, v48
	v_cvt_pk_bf16_f32 v118, v32, v33
	v_cvt_pk_bf16_f32 v119, v34, v35
	ds_read_b64_tr_b16 v[178:179], v162 offset:30720
	ds_read_b64_tr_b16 v[180:181], v162 offset:31232
	v_mfma_f32_32x32x16_bf16 v[64:79], v[154:157], v[102:105], v[64:79]
	v_add_f32_e32 v32, v38, v48
	v_add_f32_e32 v32, v39, v32
	v_add_f32_e32 v32, v40, v32
	v_add_f32_e32 v32, v41, v32
	v_cvt_pk_bf16_f32 v120, v36, v37
	v_cvt_pk_bf16_f32 v121, v38, v39
	ds_read_b64_tr_b16 v[174:175], v162 offset:27648
	ds_read_b64_tr_b16 v[176:177], v162 offset:28160
	v_mfma_f32_32x32x16_bf16 v[80:95], v[166:169], v[98:101], v[80:95]
	v_add_f32_e32 v32, v42, v32
	v_add_f32_e32 v32, v43, v32
	v_add_f32_e32 v32, v44, v32
	v_add_f32_e32 v32, v45, v32
	v_cvt_pk_bf16_f32 v114, v40, v41
	v_cvt_pk_bf16_f32 v115, v42, v43
	ds_read_b64_tr_b16 v[170:171], v162 offset:31744
	ds_read_b64_tr_b16 v[172:173], v162 offset:32256
	v_mfma_f32_32x32x16_bf16 v[64:79], v[150:153], v[98:101], v[64:79]
	v_add_f32_e32 v32, v46, v32
	v_add_f32_e32 v32, v47, v32
	v_add_f32_e64 v240, v224, v32
	v_cvt_pk_bf16_f32 v116, v44, v45
	v_cvt_pk_bf16_f32 v117, v46, v47
	s_waitcnt lgkmcnt(14)
	s_nop 0
	ds_read_b128 v[32:35], v205 offset:256
	ds_read_b128 v[36:39], v205 offset:288
	ds_read_b128 v[50:53], v205 offset:384
	ds_read_b128 v[54:57], v205 offset:416
	ds_read_b128 v[40:43], v205 offset:320
	ds_read_b128 v[44:47], v205 offset:352
	ds_read_b128 v[58:61], v205 offset:448
	ds_read_b128 v[162:165], v205 offset:480
	v_max_f32_e64 v48, v80, v81
	v_max3_f32 v49, v82, v83, v84
	v_max3_f32 v48, v48, v85, v86
	v_max3_f32 v49, v49, v87, v88
	v_max3_f32 v48, v48, v89, v90
	v_max3_f32 v49, v49, v91, v92
	v_max3_f32 v48, v48, v93, v94
	v_max3_f32 v49, v49, v95, v64
	v_max3_f32 v48, v48, v65, v66
	v_max3_f32 v49, v49, v67, v68
	v_max3_f32 v48, v48, v69, v70
	v_max3_f32 v49, v49, v71, v72
	v_max3_f32 v48, v48, v73, v74
	v_max3_f32 v49, v49, v75, v76
	v_max3_f32 v48, v48, v77, v78
	v_max3_f32 v48, v48, v79, v49
	v_mov_b32_e64 v49, v48
	s_nop 1
	v_permlane32_swap_b32_e32 v48, v49
	v_max_f32_e32 v48, v48, v49
	v_cmp_lt_f32_e32 vcc, s51, v48
	s_mov_b64 s[18:19], 0
	s_cbranch_vccnz .LBB0_737
